# n25_ld4_al16
# speedup vs baseline: 1.0059x; 1.0019x over previous
.LBB2_15:
	v_ashrrev_i32_e32 v163, 31, v162
	v_lshl_or_b32 v164, s30, 4, v132
	v_lshlrev_b64 v[130:131], 11, v[162:163]
	v_mov_b32_e32 v167, 0
	s_waitcnt lgkmcnt(0)
	s_mov_b64 s[50:51], s[0:1]
	v_lshl_add_u64 v[130:131], s[0:1], 0, v[130:131]
	v_lshlrev_b32_e32 v166, 4, v164
	v_lshl_add_u64 v[168:169], v[130:131], 0, v[166:167]
	global_load_dwordx2 v[170:171], v[168:169], off nt
	v_lshlrev_b32_e32 v142, 4, v140
	v_cmp_gt_u32_e64 s[2:3], 16, v140
	v_mov_b32_e32 v140, 0x10000
	v_lshlrev_b32_e32 v130, 8, v139
	v_lshlrev_b32_e32 v131, 4, v132
	v_lshlrev_b32_e32 v132, 3, v138
	v_lshl_or_b32 v177, v138, 14, v142
	v_lshl_or_b32 v139, v139, 11, v140
	v_lshlrev_b32_e32 v140, 10, v138
	v_xor_b32_e32 v138, 1, v138
	v_lshlrev_b32_e32 v141, 12, v1
	v_lshlrev_b32_e32 v138, 10, v138
	v_or3_b32 v179, v139, v138, v142
	v_add_u32_e32 v138, 0x1000, v141
	v_and_b32_e32 v180, 0x3000, v138
	v_add_u32_e32 v138, 0x1400, v141
	v_and_b32_e32 v181, 0x3400, v138
	v_add_u32_e32 v138, 0x1800, v141
	v_and_b32_e32 v182, 0x3800, v138
	v_add_u32_e32 v138, 0x1c00, v141
	v_and_b32_e32 v183, 0x3c00, v138
	s_movk_i32 s4, 0x2000
	v_mov_b32_e32 v138, 0x3000
	v_bitop3_b32 v184, v141, s4, v138 bitop3:0x6c
	v_add_u32_e32 v138, 0x2400, v141
	v_and_b32_e32 v185, 0x3400, v138
	v_add_u32_e32 v138, 0x2800, v141
	v_and_b32_e32 v186, 0x3800, v138
	v_add_u32_e32 v138, 0x2c00, v141
	v_and_b32_e32 v187, 0x3c00, v138
	v_add_u32_e32 v138, 0x3000, v141
	v_and_b32_e32 v188, 0x3000, v138
	v_add_u32_e32 v138, 0x3400, v141
	s_and_b32 s9, s7, 0xffff
	v_cmp_eq_u32_e32 vcc, s14, v133
	v_lshl_or_b32 v131, s16, 10, v131
	s_movk_i32 s0, 0x100
	v_lshlrev_b32_e32 v166, 12, v164
	v_and_b32_e32 v189, 0x3400, v138
	v_add_u32_e32 v138, 0x3800, v141
	s_cmp_lg_u64 vcc, exec
	v_lshl_add_u32 v131, s30, 15, v131
	v_cmp_gt_u32_e64 s[0:1], s0, v0
	v_lshl_add_u64 v[0:1], s[12:13], 0, v[166:167]
	v_and_b32_e32 v190, 0x3800, v138
	v_add_u32_e32 v138, 0x3c00, v141
	v_mov_b32_e32 v172, -1
	s_mov_b32 s11, 0x20000
	s_mov_b32 s10, 0x200400
	s_mov_b32 s8, s6
	s_cselect_b64 s[14:15], -1, 0
	v_or3_b32 v165, v131, v132, v130
	s_mov_b32 s17, 0
	v_cndmask_b32_e64 v133, 0, v137, s[0:1]
	v_cndmask_b32_e64 v132, 0, v136, s[0:1]
	v_cndmask_b32_e64 v131, 0, v135, s[0:1]
	v_cndmask_b32_e64 v130, 0, v134, s[0:1]
	v_cndmask_b32_e64 v137, v137, 0, s[0:1]
	v_cndmask_b32_e64 v136, v136, 0, s[0:1]
	v_cndmask_b32_e64 v135, v135, 0, s[0:1]
	v_cndmask_b32_e64 v134, v134, 0, s[0:1]
	v_or_b32_e32 v176, v141, v142
	v_lshl_add_u64 v[0:1], v[162:163], 2, v[0:1]
	v_or3_b32 v178, v139, v140, v142
	v_and_b32_e32 v191, 0x3c00, v138
	s_mov_b64 s[24:25], 0
	s_mov_b64 s[18:19], 0x400
	s_mov_b64 s[20:21], 0x800
	s_mov_b64 s[22:23], 0xc00
	s_mov_b32 s31, 0x40004000
	v_mov_b32_e32 v173, v172
	v_mov_b32_e32 v192, 0
	v_mov_b32_e32 v193, 0
	s_mov_b32 s33, 0
	v_add_u32_e32 v180, v180, v177
	v_add_u32_e32 v181, v181, v177
	v_add_u32_e32 v182, v182, v177
	v_add_u32_e32 v183, v183, v177
	v_add_u32_e32 v184, v184, v177
	v_add_u32_e32 v185, v185, v177
	v_add_u32_e32 v186, v186, v177
	v_add_u32_e32 v187, v187, v177
	v_add_u32_e32 v188, v188, v177
	v_add_u32_e32 v189, v189, v177
	v_add_u32_e32 v190, v190, v177
	v_add_u32_e32 v191, v191, v177
	v_mov_b32_e32 v166, v176
	v_lshlrev_b32_e32 v242, 12, v164
	v_lshl_add_u32 v242, v162, 2, v242
	v_lshlrev_b32_e32 v243, 11, v162
	v_lshl_add_u32 v243, v164, 4, v243
	v_readfirstlane_b32 s42, v176
	s_or_b32 s42, s42, 0x8000
	s_mov_b32 m0, s42
	s_lshl_b32 s36, s30, 15
	s_add_u32 s54, s6, s36
	s_addc_u32 s55, s7, 0
	s_mov_b64 s[40:41], s[54:55]
	s_mov_b32 s45, 0
	s_mov_b32 s58, 0x40000
	s_mov_b32 s46, 0x180000
	s_mov_b64 s[48:49], s[12:13]
	s_cmp_lg_u64 s[14:15], 0
	s_cselect_b32 s57, 1, 0
	s_cmp_lg_u64 s[0:1], 0
	s_cselect_b32 s59, 1, 0
	s_mov_b32 s47, 0
	s_mov_b32 s60, 0
	s_mov_b32 s44, 0
	s_add_u32 s52, s50, 8
	s_addc_u32 s53, s51, 0
	global_load_dwordx2 v[174:175], v243, s[52:53] nt
	s_add_u32 s52, s50, 0x200000
	s_addc_u32 s53, s51, 0
	s_waitcnt vmcnt(1)
	v_cvt_f32_f16_e32 v250, v170
	v_cvt_f32_f16_sdwa v251, v170 dst_sel:DWORD dst_unused:UNUSED_PAD src0_sel:WORD_1
	v_cvt_f32_f16_e32 v252, v171
	v_cvt_f32_f16_sdwa v253, v171 dst_sel:DWORD dst_unused:UNUSED_PAD src0_sel:WORD_1
	v_pk_add_f32 v[198:199], v[130:131], v[134:135]
	v_pk_add_f32 v[200:201], v[132:133], v[136:137]
	v_mov_b32_e32 v194, 0
	v_mov_b32_e32 v195, 0
	v_mov_b32_e32 v196, 0
	v_mov_b32_e32 v197, 0
	v_pk_add_f32 v[198:199], v[198:199], v[250:251]
	v_pk_add_f32 v[200:201], v[200:201], v[252:253]
	s_branch .Lrec_act
	s_nop 0
	s_nop 0
	s_nop 0
	s_nop 0
